# v045 + grid barrier pre-flush: the arrivers with 1 and 8 workgroups of their XCD still missing issue a fire-and-forget buffer_wbl2
# speedup vs baseline: 1.0011x; 1.0011x over previous
; __device__ __forceinline__ unsigned xb_ld(unsigned* p)              { return __hip_atomic_load(p, __ATOMIC_RELAXED, __HIP_MEMORY_SCOPE_AGENT); }
; __device__ __forceinline__ unsigned xb_add(unsigned* p, unsigned v) { return __hip_atomic_fetch_add(p, v, __ATOMIC_RELAXED, __HIP_MEMORY_SCOPE_AGENT); }
; #define XB_SPIN(cond, bar) do { unsigned _sp = 0; while (cond) { __builtin_amdgcn_s_sleep(1); \
;     if ((++_sp & 255u) == 0u) { if (xb_ld(&(bar)[XB_TMO])) break; if (_sp > XB_SPIN_CAP) { atomicAdd(&(bar)[XB_TMO], 1u); break; } } } } while (0)
; __device__ __forceinline__ void xcd_barrier(const XcdBarrier& b) {
;     ...
;         const unsigned old = xb_add(&bar[XB_XSUB(b.x)], 1u);
;         const unsigned gen = old / nloc;
;         if (old + 1u == (gen + 1u) * nloc) {
;     ...
;         } else {
;             XB_SPIN(xb_ld(&bar[XB_XGEN(b.x)]) == gen, bar);
;             __builtin_amdgcn_fence(__ATOMIC_ACQUIRE, "agent");
.LBB0_80:
	s_or_b64 exec, exec, s[10:11]
	v_cvt_f32_u32_e32 v5, v3
	s_waitcnt vmcnt(0)
	v_readfirstlane_b32 s3, v4
	v_sub_u32_e32 v4, 0, v3
	v_rcp_iflag_f32_e32 v5, v5
	v_add_u32_e32 v6, s3, v2
	v_mul_f32_e32 v5, 0x4f7ffffe, v5
	v_cvt_u32_f32_e32 v5, v5
	v_mul_lo_u32 v2, v4, v5
	v_mul_hi_u32 v2, v5, v2
	v_add_u32_e32 v2, v5, v2
	v_mul_hi_u32 v2, v6, v2
	v_mul_lo_u32 v4, v2, v3
	v_sub_u32_e32 v4, v6, v4
	v_add_u32_e32 v5, 1, v2
	v_cmp_ge_u32_e32 vcc, v4, v3
	s_nop 1
	v_cndmask_b32_e32 v2, v2, v5, vcc
	v_sub_u32_e32 v5, v4, v3
	v_cndmask_b32_e32 v4, v4, v5, vcc
	v_add_u32_e32 v5, 1, v2
	v_cmp_ge_u32_e32 vcc, v4, v3
	v_add_u32_e32 v4, 1, v6
	s_nop 0
	v_cndmask_b32_e32 v2, v2, v5, vcc
	v_mul_lo_u32 v5, v3, v2
	v_add_u32_e32 v3, v5, v3
	v_cmp_ne_u32_e32 vcc, v4, v3
	s_and_saveexec_b64 s[8:9], vcc
	s_xor_b64 s[8:9], exec, s[8:9]
	s_cbranch_execz .LBB0_94
	s_waitcnt lgkmcnt(0)
	v_sub_u32_e32 v7, v3, v4
	v_mov_b32_e32 v8, 0x102
	v_lshrrev_b32_e32 v8, v7, v8
	v_and_b32_e32 v8, 1, v8
	v_cmp_eq_u32_e32 vcc, 1, v8
	s_cbranch_vccz .Lpfl_0
	buffer_wbl2 sc1
.Lpfl_0:
	buffer_inv sc1
	v_mov_b32_e32 v1, 0x2000
	global_load_dword v1, v1, s[6:7] offset:1024 sc1
	s_add_u32 s12, s6, 0x2400
	s_addc_u32 s13, s7, 0
	s_waitcnt vmcnt(0)
	v_cmp_eq_u32_e32 vcc, v1, v2
	s_and_saveexec_b64 s[10:11], vcc
	s_cbranch_execz .LBB0_93
	s_mov_b32 s3, 1
	s_mov_b64 s[14:15], 0
	v_mov_b32_e32 v1, 0
	s_branch .LBB0_84

; __device__ __forceinline__ unsigned xb_ld(unsigned* p)              { return __hip_atomic_load(p, __ATOMIC_RELAXED, __HIP_MEMORY_SCOPE_AGENT); }
; __device__ __forceinline__ unsigned xb_add(unsigned* p, unsigned v) { return __hip_atomic_fetch_add(p, v, __ATOMIC_RELAXED, __HIP_MEMORY_SCOPE_AGENT); }
; #define XB_SPIN(cond, bar) do { unsigned _sp = 0; while (cond) { __builtin_amdgcn_s_sleep(1); \
;     if ((++_sp & 255u) == 0u) { if (xb_ld(&(bar)[XB_TMO])) break; if (_sp > XB_SPIN_CAP) { atomicAdd(&(bar)[XB_TMO], 1u); break; } } } } while (0)
; __device__ __forceinline__ void xcd_barrier(const XcdBarrier& b) {
;     ...
;         const unsigned old = xb_add(&bar[XB_XSUB(b.x)], 1u);
;         const unsigned gen = old / nloc;
;         if (old + 1u == (gen + 1u) * nloc) {
;     ...
;         } else {
;             XB_SPIN(xb_ld(&bar[XB_XGEN(b.x)]) == gen, bar);
;             __builtin_amdgcn_fence(__ATOMIC_ACQUIRE, "agent");
.LBB0_141:
	s_or_b64 exec, exec, s[6:7]
	v_cvt_f32_u32_e32 v5, v3
	s_waitcnt vmcnt(0)
	v_readfirstlane_b32 s4, v4
	v_sub_u32_e32 v4, 0, v3
	v_rcp_iflag_f32_e32 v5, v5
	v_add_u32_e32 v6, s4, v2
	v_mul_f32_e32 v5, 0x4f7ffffe, v5
	v_cvt_u32_f32_e32 v5, v5
	v_mul_lo_u32 v2, v4, v5
	v_mul_hi_u32 v2, v5, v2
	v_add_u32_e32 v2, v5, v2
	v_mul_hi_u32 v2, v6, v2
	v_mul_lo_u32 v4, v2, v3
	v_sub_u32_e32 v4, v6, v4
	v_add_u32_e32 v5, 1, v2
	v_cmp_ge_u32_e32 vcc, v4, v3
	s_nop 1
	v_cndmask_b32_e32 v2, v2, v5, vcc
	v_sub_u32_e32 v5, v4, v3
	v_cndmask_b32_e32 v4, v4, v5, vcc
	v_add_u32_e32 v5, 1, v2
	v_cmp_ge_u32_e32 vcc, v4, v3
	v_add_u32_e32 v4, 1, v6
	s_nop 0
	v_cndmask_b32_e32 v2, v2, v5, vcc
	v_mul_lo_u32 v5, v3, v2
	v_add_u32_e32 v3, v5, v3
	v_cmp_ne_u32_e32 vcc, v4, v3
	s_and_saveexec_b64 s[4:5], vcc
	s_xor_b64 s[4:5], exec, s[4:5]
	s_cbranch_execz .LBB0_155
	s_waitcnt lgkmcnt(0)
	v_sub_u32_e32 v7, v3, v4
	v_mov_b32_e32 v8, 0x102
	v_lshrrev_b32_e32 v8, v7, v8
	v_and_b32_e32 v8, 1, v8
	v_cmp_eq_u32_e32 vcc, 1, v8
	s_cbranch_vccz .Lpfl_1
	buffer_wbl2 sc1
.Lpfl_1:
	buffer_inv sc1
	v_mov_b32_e32 v1, 0x2000
	global_load_dword v1, v1, s[2:3] offset:1024 sc1
	s_add_u32 s8, s2, 0x2400
	s_addc_u32 s9, s3, 0
	s_waitcnt vmcnt(0)
	v_cmp_eq_u32_e32 vcc, v1, v2
	s_and_saveexec_b64 s[6:7], vcc
	s_cbranch_execz .LBB0_154
	s_mov_b32 s22, 1
	s_mov_b64 s[12:13], 0
	v_mov_b32_e32 v1, 0
	s_branch .LBB0_145

; __device__ __forceinline__ unsigned xb_ld(unsigned* p)              { return __hip_atomic_load(p, __ATOMIC_RELAXED, __HIP_MEMORY_SCOPE_AGENT); }
; __device__ __forceinline__ unsigned xb_add(unsigned* p, unsigned v) { return __hip_atomic_fetch_add(p, v, __ATOMIC_RELAXED, __HIP_MEMORY_SCOPE_AGENT); }
; #define XB_SPIN(cond, bar) do { unsigned _sp = 0; while (cond) { __builtin_amdgcn_s_sleep(1); \
;     if ((++_sp & 255u) == 0u) { if (xb_ld(&(bar)[XB_TMO])) break; if (_sp > XB_SPIN_CAP) { atomicAdd(&(bar)[XB_TMO], 1u); break; } } } } while (0)
; __device__ __forceinline__ void xcd_barrier(const XcdBarrier& b) {
;     ...
;         const unsigned old = xb_add(&bar[XB_XSUB(b.x)], 1u);
;         const unsigned gen = old / nloc;
;         if (old + 1u == (gen + 1u) * nloc) {
;     ...
;         } else {
;             XB_SPIN(xb_ld(&bar[XB_XGEN(b.x)]) == gen, bar);
;             __builtin_amdgcn_fence(__ATOMIC_ACQUIRE, "agent");
.LBB0_241:
	s_or_b64 exec, exec, s[14:15]
	v_cvt_f32_u32_e32 v5, v3
	s_waitcnt vmcnt(0)
	v_readfirstlane_b32 s12, v4
	v_sub_u32_e32 v4, 0, v3
	v_rcp_iflag_f32_e32 v5, v5
	v_add_u32_e32 v6, s12, v2
	v_mul_f32_e32 v5, 0x4f7ffffe, v5
	v_cvt_u32_f32_e32 v5, v5
	v_mul_lo_u32 v2, v4, v5
	v_mul_hi_u32 v2, v5, v2
	v_add_u32_e32 v2, v5, v2
	v_mul_hi_u32 v2, v6, v2
	v_mul_lo_u32 v4, v2, v3
	v_sub_u32_e32 v4, v6, v4
	v_add_u32_e32 v5, 1, v2
	v_cmp_ge_u32_e32 vcc, v4, v3
	s_nop 1
	v_cndmask_b32_e32 v2, v2, v5, vcc
	v_sub_u32_e32 v5, v4, v3
	v_cndmask_b32_e32 v4, v4, v5, vcc
	v_add_u32_e32 v5, 1, v2
	v_cmp_ge_u32_e32 vcc, v4, v3
	v_add_u32_e32 v4, 1, v6
	s_nop 0
	v_cndmask_b32_e32 v2, v2, v5, vcc
	v_mul_lo_u32 v5, v3, v2
	v_add_u32_e32 v3, v5, v3
	v_cmp_ne_u32_e32 vcc, v4, v3
	s_and_saveexec_b64 s[12:13], vcc
	s_xor_b64 s[12:13], exec, s[12:13]
	s_cbranch_execz .LBB0_255
	s_waitcnt lgkmcnt(0)
	v_sub_u32_e32 v7, v3, v4
	v_mov_b32_e32 v8, 0x102
	v_lshrrev_b32_e32 v8, v7, v8
	v_and_b32_e32 v8, 1, v8
	v_cmp_eq_u32_e32 vcc, 1, v8
	s_cbranch_vccz .Lpfl_2
	buffer_wbl2 sc1
.Lpfl_2:
	buffer_inv sc1
	v_mov_b32_e32 v1, 0x2000
	global_load_dword v1, v1, s[4:5] offset:1024 sc1
	s_add_u32 s16, s4, 0x2400
	s_addc_u32 s17, s5, 0
	s_waitcnt vmcnt(0)
	v_cmp_eq_u32_e32 vcc, v1, v2
	s_and_saveexec_b64 s[14:15], vcc
	s_cbranch_execz .LBB0_254
	s_mov_b32 s28, 1
	s_mov_b64 s[18:19], 0
	v_mov_b32_e32 v1, 0
	s_branch .LBB0_245

; __device__ __forceinline__ unsigned xb_ld(unsigned* p)              { return __hip_atomic_load(p, __ATOMIC_RELAXED, __HIP_MEMORY_SCOPE_AGENT); }
; #define XB_SPIN(cond, bar) do { unsigned _sp = 0; while (cond) { __builtin_amdgcn_s_sleep(1); \
;     if ((++_sp & 255u) == 0u) { if (xb_ld(&(bar)[XB_TMO])) break; if (_sp > XB_SPIN_CAP) { atomicAdd(&(bar)[XB_TMO], 1u); break; } } } } while (0)
; __device__ __forceinline__ void xcd_barrier(const XcdBarrier& b) {
;     ...
;             XB_SPIN(xb_ld(&bar[XB_XGEN(b.x)]) == gen, bar);
;             __builtin_amdgcn_fence(__ATOMIC_ACQUIRE, "agent");
.Lpfl_4:
	buffer_inv sc1
	v_mov_b32_e32 v1, 0x2000
	global_load_dword v1, v1, s[2:3] offset:1024 sc1
	s_add_u32 s8, s2, 0x2400
	s_addc_u32 s9, s3, 0
	s_waitcnt vmcnt(0)
	v_cmp_eq_u32_e32 vcc, v1, v2
	s_and_saveexec_b64 s[6:7], vcc
	s_cbranch_execz .LBB0_674
	s_mov_b32 s20, 1
	s_mov_b64 s[10:11], 0
	v_mov_b32_e32 v1, 0
	s_branch .LBB0_665

; __device__ __forceinline__ unsigned xb_ld(unsigned* p)              { return __hip_atomic_load(p, __ATOMIC_RELAXED, __HIP_MEMORY_SCOPE_AGENT); }
; __device__ __forceinline__ unsigned xb_add(unsigned* p, unsigned v) { return __hip_atomic_fetch_add(p, v, __ATOMIC_RELAXED, __HIP_MEMORY_SCOPE_AGENT); }
; #define XB_SPIN(cond, bar) do { unsigned _sp = 0; while (cond) { __builtin_amdgcn_s_sleep(1); \
;     if ((++_sp & 255u) == 0u) { if (xb_ld(&(bar)[XB_TMO])) break; if (_sp > XB_SPIN_CAP) { atomicAdd(&(bar)[XB_TMO], 1u); break; } } } } while (0)
; __device__ __forceinline__ void xcd_barrier(const XcdBarrier& b) {
;     ...
;         const unsigned old = xb_add(&bar[XB_XSUB(b.x)], 1u);
;         const unsigned gen = old / nloc;
;         if (old + 1u == (gen + 1u) * nloc) {
;     ...
;         } else {
;             XB_SPIN(xb_ld(&bar[XB_XGEN(b.x)]) == gen, bar);
;             __builtin_amdgcn_fence(__ATOMIC_ACQUIRE, "agent");
.LBB0_1212:
	s_or_b64 exec, exec, s[8:9]
	v_cvt_f32_u32_e32 v5, v3
	s_waitcnt vmcnt(0)
	v_readfirstlane_b32 s6, v4
	v_sub_u32_e32 v4, 0, v3
	v_rcp_iflag_f32_e32 v5, v5
	v_add_u32_e32 v6, s6, v2
	v_mul_f32_e32 v5, 0x4f7ffffe, v5
	v_cvt_u32_f32_e32 v5, v5
	v_mul_lo_u32 v2, v4, v5
	v_mul_hi_u32 v2, v5, v2
	v_add_u32_e32 v2, v5, v2
	v_mul_hi_u32 v2, v6, v2
	v_mul_lo_u32 v4, v2, v3
	v_sub_u32_e32 v4, v6, v4
	v_add_u32_e32 v5, 1, v2
	v_cmp_ge_u32_e32 vcc, v4, v3
	s_nop 1
	v_cndmask_b32_e32 v2, v2, v5, vcc
	v_sub_u32_e32 v5, v4, v3
	v_cndmask_b32_e32 v4, v4, v5, vcc
	v_add_u32_e32 v5, 1, v2
	v_cmp_ge_u32_e32 vcc, v4, v3
	v_add_u32_e32 v4, 1, v6
	s_nop 0
	v_cndmask_b32_e32 v2, v2, v5, vcc
	v_mul_lo_u32 v5, v3, v2
	v_add_u32_e32 v3, v5, v3
	v_cmp_ne_u32_e32 vcc, v4, v3
	s_and_saveexec_b64 s[6:7], vcc
	s_xor_b64 s[6:7], exec, s[6:7]
	s_cbranch_execz .LBB0_1226
	s_waitcnt lgkmcnt(0)
	v_sub_u32_e32 v7, v3, v4
	v_mov_b32_e32 v8, 0x102
	v_lshrrev_b32_e32 v8, v7, v8
	v_and_b32_e32 v8, 1, v8
	v_cmp_eq_u32_e32 vcc, 1, v8
	s_cbranch_vccz .Lpfl_8
	buffer_wbl2 sc1
.Lpfl_8:
	buffer_inv sc1
	v_mov_b32_e32 v1, 0x2000
	global_load_dword v1, v1, s[2:3] offset:1024 sc1
	s_add_u32 s10, s2, 0x2400
	s_addc_u32 s11, s3, 0
	s_waitcnt vmcnt(0)
	v_cmp_eq_u32_e32 vcc, v1, v2
	s_and_saveexec_b64 s[8:9], vcc
	s_cbranch_execz .LBB0_1225
	s_mov_b32 s22, 1
	s_mov_b64 s[12:13], 0
	v_mov_b32_e32 v1, 0
	s_branch .LBB0_1216

; __device__ __forceinline__ unsigned xb_ld(unsigned* p)              { return __hip_atomic_load(p, __ATOMIC_RELAXED, __HIP_MEMORY_SCOPE_AGENT); }
; #define XB_SPIN(cond, bar) do { unsigned _sp = 0; while (cond) { __builtin_amdgcn_s_sleep(1); \
;     if ((++_sp & 255u) == 0u) { if (xb_ld(&(bar)[XB_TMO])) break; if (_sp > XB_SPIN_CAP) { atomicAdd(&(bar)[XB_TMO], 1u); break; } } } } while (0)
; __device__ __forceinline__ void xcd_barrier(const XcdBarrier& b) {
;     ...
;             XB_SPIN(xb_ld(&bar[XB_XGEN(b.x)]) == gen, bar);
;             __builtin_amdgcn_fence(__ATOMIC_ACQUIRE, "agent");
.Lpfl_10:
	buffer_inv sc1
	v_mov_b32_e32 v1, 0x2000
	global_load_dword v1, v1, s[2:3] offset:1024 sc1
	s_add_u32 s10, s2, 0x2400
	s_addc_u32 s11, s3, 0
	s_waitcnt vmcnt(0)
	v_cmp_eq_u32_e32 vcc, v1, v2
	s_and_saveexec_b64 s[8:9], vcc
	s_cbranch_execz .LBB0_1756
	s_mov_b32 s26, 1
	s_mov_b64 s[12:13], 0
	v_mov_b32_e32 v1, 0
	s_branch .LBB0_1747

; __device__ __forceinline__ unsigned xb_ld(unsigned* p)              { return __hip_atomic_load(p, __ATOMIC_RELAXED, __HIP_MEMORY_SCOPE_AGENT); }
; #define XB_SPIN(cond, bar) do { unsigned _sp = 0; while (cond) { __builtin_amdgcn_s_sleep(1); \
;     if ((++_sp & 255u) == 0u) { if (xb_ld(&(bar)[XB_TMO])) break; if (_sp > XB_SPIN_CAP) { atomicAdd(&(bar)[XB_TMO], 1u); break; } } } } while (0)
; __device__ __forceinline__ void xcd_barrier(const XcdBarrier& b) {
;     ...
;             XB_SPIN(xb_ld(&bar[XB_XGEN(b.x)]) == gen, bar);
;             __builtin_amdgcn_fence(__ATOMIC_ACQUIRE, "agent");
.Lpfl_11:
	buffer_inv sc1
	v_mov_b32_e32 v1, 0x2000
	global_load_dword v1, v1, s[2:3] offset:1024 sc1
	s_add_u32 s10, s2, 0x2400
	s_addc_u32 s11, s3, 0
	s_waitcnt vmcnt(0)
	v_cmp_eq_u32_e32 vcc, v1, v2
	s_and_saveexec_b64 s[8:9], vcc
	s_cbranch_execz .LBB0_1839
	s_mov_b32 s24, 1
	s_mov_b64 s[12:13], 0
	v_mov_b32_e32 v1, 0
	s_branch .LBB0_1830
